# v029 plus attention body prologue: the V-keys-32..63 loads issued together with the K/V-first-half loads ahead of the single vmcnt(0) (one exposed round trip per body instead of two)
# speedup vs baseline: 1.0227x; 1.0096x over previous
; __device__ __forceinline__ int v_rd_base(int lane) { return ((lane & 3) << 3) | (((lane >> 2) & 3) << 6) | (((lane >> 4) & 1) << 5) | (((lane >> 5) & 1) << 8); }
; __device__ __forceinline__ int v_st256(int k, int c) { const int kk = (k & ~0xC) | ((k & 4) << 1) | ((k & 8) >> 1); return ((kk >> 3) * 8 + (c >> 5)) * 512 + ((kk & 7) * 32 + (c & 31)) * 2; }
; #define SLOAD_A(k0) do { const bf16_t* vp_ = Vh + (long)(k0) * LDK + toff; const bf16_t* kp_ = Kh + (long)(k0) * LDK + toff; \
;     sa0 = *(const bf16x8*)kp_; sa1 = *(const bf16x8*)(kp_ + 32L * LDK); sa2 = *(const bf16x8*)vp_; sa3 = *(const bf16x8*)(vp_ + 128); } while (0)
; #define SWRITE_A(b) do { LAS char* vb_ = V_lds + (b) * SHM_V2 + vst00; LAS char* kb_ = K_lds + (b) * SHM_K2 + kst0; \
;     *(LAS bf16x8*)(kb_) = sa0; *(LAS bf16x8*)(kb_ + 8192) = sa1; *(LAS bf16x8*)(vb_) = sa2; *(LAS bf16x8*)(vb_ + 2048) = sa3; } while (0)
; #define SLOAD_B(k0) do { const bf16_t* vp_ = Vh + (long)((k0) + 32) * LDK + toff; sa0 = *(const bf16x8*)vp_; sa1 = *(const bf16x8*)(vp_ + 128); } while (0)
; #define SWRITE_B(b) do { LAS char* vb_ = V_lds + (b) * SHM_V2 + vst00; *(LAS bf16x8*)(vb_ + 16384) = sa0; *(LAS bf16x8*)(vb_ + 18432) = sa1; } while (0)
; template <int LDQ, int LDK, int LDO>
; __device__ __forceinline__ void attn_body256(const bf16_t* __restrict__ Qb, const bf16_t* __restrict__ Kh, const bf16_t* __restrict__ Vh, float* __restrict__ Ob, int seq, LAS char* lds) {
;     ...
;   float m_reg = -1e30f, l_reg = 0; f32x16 o[8] = {}; bf16x8 qr[8];
;   const bf16_t* Qw = Qb + (long)(wid * QBLK + r32) * LDQ + hi * 8;
; #pragma unroll
;   for (int d0 = 0; d0 < 8; ++d0) qr[d0] = *(const bf16x8*)(Qw + d0 * 16);
;   const int sr = tid >> 4, sc = (tid & 15) * 8;
;   const int vst00 = v_st256(sr, sc), kst0 = KSWZ(sr, sc * 2);
;   const unsigned toff = (unsigned)(sr * LDK + sc);
;   const int vb0 = (int)(uintptr_t)V_lds + v_rd_base(lane);
;   bf16x8 sa0, sa1, sa2, sa3;
;     ...
;   f32x16 p0, p1; float mn, al; bf16x8 pa0, pa1, pa2, pa3; const int NT = seq / KVBLK;
;   SLOAD_A(0); asm volatile("s_waitcnt vmcnt(0)" ::: "memory"); SWRITE_A(0); SLOAD_B(0); asm volatile("s_waitcnt vmcnt(0)" ::: "memory"); SWRITE_B(0); __syncthreads();
.LBB0_933:
	s_lshl_b64 s[8:9], s[10:11], 1
	s_add_u32 s6, s4, s8
	s_addc_u32 s7, s5, s9
	v_mov_b32_e32 v226, v241
	s_movk_i32 s82, 0xffe0
	v_ashrrev_i32_e32 v17, 1, v241
	v_bfe_u32 v231, v241, 5, 1
	v_bfi_b32 v2, s82, v17, v241
	v_mov_b64_e32 v[4:5], s[6:7]
	s_movk_i32 s6, 0x3080
	v_mad_i64_i32 v[4:5], s[6:7], v2, s6, v[4:5]
	v_lshlrev_b32_e32 v212, 4, v231
	v_mov_b32_e32 v213, v3
	v_lshlrev_b32_e32 v19, 3, v241
	v_lshl_add_u64 v[4:5], v[4:5], 0, v[212:213]
	v_ashrrev_i32_e32 v18, 4, v241
	v_and_b32_e32 v2, 0x78, v19
	s_movk_i32 s6, 0x1840
	global_load_dwordx4 v[164:167], v[4:5], off
	global_load_dwordx4 v[168:171], v[4:5], off offset:32
	global_load_dwordx4 v[172:175], v[4:5], off offset:64
	global_load_dwordx4 v[176:179], v[4:5], off offset:96
	global_load_dwordx4 v[180:183], v[4:5], off offset:128
	global_load_dwordx4 v[184:187], v[4:5], off offset:160
	global_load_dwordx4 v[188:191], v[4:5], off offset:192
	global_load_dwordx4 v[192:195], v[4:5], off offset:224
	v_mad_u64_u32 v[4:5], s[6:7], v18, s6, v[2:3]
	s_add_u32 s10, s16, s8
	v_mov_b32_e32 v5, v3
	s_addc_u32 s11, s17, s9
	v_lshlrev_b64 v[12:13], 1, v[4:5]
	v_lshl_add_u64 v[4:5], s[10:11], 0, v[12:13]
	s_mov_b32 s6, 0x61000
	s_waitcnt vmcnt(10)
	v_add_co_u32_e32 v8, vcc, s6, v4
	v_lshl_add_u64 v[14:15], s[18:19], 0, v[12:13]
	s_nop 0
	v_addc_co_u32_e32 v9, vcc, 0, v5, vcc
	global_load_dwordx4 v[4:7], v[4:5], off
	s_nop 0
	global_load_dwordx4 v[8:11], v[8:9], off
	s_nop 0
	global_load_dwordx4 v[196:199], v[14:15], off
	global_load_dwordx4 v[200:203], v[14:15], off offset:256
	v_lshl_add_u64 v[14:15], s[24:25], 0, v[12:13]
	global_load_dwordx4 v[204:207], v[14:15], off
	global_load_dwordx4 v[208:211], v[14:15], off offset:256
	s_waitcnt vmcnt(0)
	v_and_b32_e32 v15, 0x3fffffc0, v241
	v_lshlrev_b32_e32 v20, 4, v241
	v_and_b32_e32 v214, 0xffffffe0, v17
	v_lshlrev_b32_e32 v17, 1, v18
	v_lshl_add_u32 v232, v15, 2, s64
	v_and_b32_e32 v15, 3, v18
	v_lshrrev_b32_e32 v22, 1, v18
	v_and_b32_e32 v23, 0x7ffff0, v18
	v_bfe_u32 v24, v19, 5, 2
	v_and_b32_e32 v26, 0x70, v20
	v_and_b32_e32 v17, 8, v17
	v_lshlrev_b32_e32 v2, 1, v2
	s_movk_i32 s7, 0x60
	v_lshlrev_b32_e32 v21, 1, v241
	v_lshlrev_b32_e32 v18, 8, v18
	v_and_b32_e32 v25, 0xc0, v20
	v_and_or_b32 v15, v22, 4, v15
	s_add_i32 s6, 0, 0x10000
	v_bitop3_b32 v215, v212, v20, s65 bitop3:0x78
	v_bitop3_b32 v235, v212, v26, s7 bitop3:0x36
	s_movk_i32 s7, 0x80
	v_or3_b32 v17, v23, v17, v24
	v_and_b32_e32 v20, 48, v2
	v_bitop3_b32 v2, v2, v241, s65 bitop3:0x78
	v_and_b32_e32 v213, 31, v241
	v_and_b32_e32 v21, 32, v21
	v_bitop3_b32 v236, v212, v26, s7 bitop3:0x36
	s_movk_i32 s7, 0xa0
	v_lshlrev_b32_e32 v15, 6, v15
	v_lshl_add_u32 v16, v17, 9, 0
	v_add3_u32 v240, s6, v2, v18
	s_movk_i32 s11, 0x118
	s_add_u32 s8, s78, s8
	v_and_b32_e32 v14, 63, v241
	v_bitop3_b32 v237, v212, v26, s7 bitop3:0x36
	s_movk_i32 s7, 0xc0
	v_lshl_add_u32 v239, v213, 8, s6
	v_add3_u32 v241, v16, v15, v20
	s_movk_i32 s6, 0xe0
	v_and_or_b32 v2, v19, s11, v21
	s_addc_u32 s9, s79, s9
	v_mov_b32_e32 v16, v3
	v_mov_b32_e32 v17, v3
	v_bitop3_b32 v233, v212, v26, 32 bitop3:0x36
	v_bitop3_b32 v234, v212, v26, 64 bitop3:0x36
	v_bitop3_b32 v238, v212, v26, s7 bitop3:0x36
	v_bitop3_b32 v242, v212, v26, s6 bitop3:0x36
	v_cmp_gt_u32_e64 s[6:7], 32, v14
	v_add3_u32 v244, v25, 0, v2
	v_lshl_add_u64 v[216:217], s[78:79], 0, v[12:13]
	v_lshl_add_u64 v[218:219], s[8:9], 0, v[12:13]
	v_mov_b32_e32 v2, v3
	v_mov_b32_e32 v12, v3
	v_mov_b32_e32 v13, v3
	s_waitcnt vmcnt(5)
	ds_write_b128 v240, v[4:7]
	s_waitcnt vmcnt(4)
	ds_write_b128 v240, v[8:11] offset:8192
	s_waitcnt vmcnt(3)
	ds_write_b128 v241, v[196:199]
	s_waitcnt vmcnt(2)
	ds_write_b128 v241, v[200:203] offset:2048
	s_waitcnt vmcnt(0)
	v_mov_b32_e32 v4, v3
	v_mov_b32_e32 v5, v3
	v_mov_b32_e32 v6, v3
	v_mov_b32_e32 v7, v3
	v_mov_b32_e32 v8, v3
	v_mov_b32_e32 v9, v3
	v_mov_b32_e32 v10, v3
	v_mov_b32_e32 v11, v3
	v_mov_b32_e32 v14, v3
	v_mov_b32_e32 v15, v3
	v_mov_b64_e32 v[130:131], v[16:17]
	v_mov_b64_e32 v[114:115], v[16:17]
	v_mov_b64_e32 v[98:99], v[16:17]
	v_mov_b64_e32 v[82:83], v[16:17]
	v_mov_b64_e32 v[66:67], v[16:17]
	v_mov_b64_e32 v[50:51], v[16:17]
	v_mov_b64_e32 v[34:35], v[16:17]
	v_mov_b64_e32 v[128:129], v[14:15]
	v_mov_b64_e32 v[126:127], v[12:13]
	v_mov_b64_e32 v[124:125], v[10:11]
	v_mov_b64_e32 v[122:123], v[8:9]
	v_mov_b64_e32 v[120:121], v[6:7]
	v_mov_b64_e32 v[118:119], v[4:5]
	v_mov_b64_e32 v[116:117], v[2:3]
	v_mov_b64_e32 v[112:113], v[14:15]
	v_mov_b64_e32 v[110:111], v[12:13]
	v_mov_b64_e32 v[108:109], v[10:11]
	v_mov_b64_e32 v[106:107], v[8:9]
	v_mov_b64_e32 v[104:105], v[6:7]
	v_mov_b64_e32 v[102:103], v[4:5]
	v_mov_b64_e32 v[100:101], v[2:3]
	v_mov_b64_e32 v[96:97], v[14:15]
	v_mov_b64_e32 v[94:95], v[12:13]
	v_mov_b64_e32 v[92:93], v[10:11]
	v_mov_b64_e32 v[90:91], v[8:9]
	v_mov_b64_e32 v[88:89], v[6:7]
	v_mov_b64_e32 v[86:87], v[4:5]
	v_mov_b64_e32 v[84:85], v[2:3]
	v_mov_b64_e32 v[80:81], v[14:15]
	v_mov_b64_e32 v[78:79], v[12:13]
	v_mov_b64_e32 v[76:77], v[10:11]
	v_mov_b64_e32 v[74:75], v[8:9]
	v_mov_b64_e32 v[72:73], v[6:7]
	v_mov_b64_e32 v[70:71], v[4:5]
	v_mov_b64_e32 v[68:69], v[2:3]
	v_mov_b64_e32 v[64:65], v[14:15]
	v_mov_b64_e32 v[62:63], v[12:13]
	v_mov_b64_e32 v[60:61], v[10:11]
	v_mov_b64_e32 v[58:59], v[8:9]
	v_mov_b64_e32 v[56:57], v[6:7]
	v_mov_b64_e32 v[54:55], v[4:5]
	v_mov_b64_e32 v[52:53], v[2:3]
	v_mov_b64_e32 v[48:49], v[14:15]
	v_mov_b64_e32 v[46:47], v[12:13]
	v_mov_b64_e32 v[44:45], v[10:11]
	v_mov_b64_e32 v[42:43], v[8:9]
	v_mov_b64_e32 v[40:41], v[6:7]
	v_mov_b64_e32 v[38:39], v[4:5]
	v_mov_b64_e32 v[36:37], v[2:3]
	v_mov_b64_e32 v[32:33], v[14:15]
	v_mov_b64_e32 v[30:31], v[12:13]
	v_mov_b64_e32 v[28:29], v[10:11]
	v_mov_b64_e32 v[26:27], v[8:9]
	v_mov_b64_e32 v[24:25], v[6:7]
	v_mov_b64_e32 v[22:23], v[4:5]
	v_mov_b64_e32 v[20:21], v[2:3]
	v_mov_b64_e32 v[18:19], v[16:17]
	s_mov_b32 s10, 0
	v_lshl_add_u32 v243, v213, 2, v232
	v_mov_b32_e32 v245, 0
	v_mov_b32_e32 v248, 0xf149f2ca
	s_mov_b64 s[82:83], 0
	s_mov_b32 s86, 0x8000
	v_mov_b64_e32 v[16:17], v[14:15]
	v_mov_b64_e32 v[14:15], v[12:13]
	v_mov_b64_e32 v[12:13], v[10:11]
	v_mov_b64_e32 v[10:11], v[8:9]
	v_mov_b64_e32 v[8:9], v[6:7]
	v_mov_b64_e32 v[6:7], v[4:5]
	v_mov_b64_e32 v[4:5], v[2:3]
	s_waitcnt vmcnt(1)
	ds_write_b128 v241, v[204:207] offset:16384
	s_waitcnt vmcnt(0)
	ds_write_b128 v241, v[208:211] offset:18432
	s_waitcnt lgkmcnt(0)
	s_barrier
